# mLSTM state-update block: B fragments requested 3-4 MFMAs ahead with counted lgkmcnt instead of read-wait-MFMA
# baseline (speedup 1.0000x reference)
; #define WG_BAR() do { asm volatile("s_waitcnt lgkmcnt(0)" ::: "memory"); __builtin_amdgcn_s_barrier(); asm volatile("" ::: "memory"); } while (0)
; template <bool OUT, bool PASS2>
; __device__ __forceinline__ void ml_block(const Args& a, unsigned char* lds_g, int rowbase, int h, int dir, f32x4 (&st)[9], int tid) {
;     ...
;             for (int ks = 0; ks < 2; ++ks) { const bf16x8_t kf = frag_tr(Ki, ML_STRIDE, 32 * ks, 16 * w, lane);
; #pragma unroll
;                 for (int vt = 0; vt < 8; ++vt) st[vt] = __builtin_amdgcn_mfma_f32_16x16x32_bf16(kf, frag_tr(Vi, ML_STRIDE, 32 * ks, 16 * vt, lane), st[vt], 0, 0, 0);
;                 st[8] = __builtin_amdgcn_mfma_f32_16x16x32_bf16(kf, frag_tr(AUGi, 16, 32 * ks, 0, lane), st[8], 0, 0, 0); }
;             const float ee = ebend[c];
; #pragma unroll
;             for (int vt = 0; vt < 9; ++vt) st[vt] = st[vt] * ee;
;         }
;         WG_BAR();
;         if (OUT) {
;             float sq[4] = {0.f, 0.f, 0.f, 0.f};
; #pragma unroll
;             for (int r = 0; r < 4; ++r) { const int t = 16 * ti + 4 * fq + r; const float sc = eb[64 * c + t] * __builtin_amdgcn_rcpf(fmaxf(fabsf(den[t]), 1.f));
; #pragma unroll
;                 for (int x = 0; x < 4; ++x) { const int vt = vh * 5 + x; const float hv = (vt < 8) ? X[x][r] * sc : 0.f; hval[x][r] = hv; sq[r] += hv * hv; }
;                 if (vh == 0) { const float hv = X[4][r] * sc; X[4][r] = hv; sq[r] += hv * hv; } }
; #pragma unroll
;             for (int r = 0; r < 4; ++r) { float v = sq[r]; v += __shfl_xor(v, 1); v += __shfl_xor(v, 2); v += __shfl_xor(v, 4); v += __shfl_xor(v, 8); if (fr == 0) ssq[vh * 64 + 16 * ti + 4 * fq + r] = v; }
.LBB0_494:
	s_or_b64 exec, exec, s[30:31]
	ds_read_b64_tr_b16 v[80:81], v195 offset:17408
	ds_read_b64_tr_b16 v[82:83], v195 offset:18496
	ds_read_b64_tr_b16 v[84:85], v157 offset:34816
	ds_read_b64_tr_b16 v[86:87], v157 offset:35904
	ds_read_b64_tr_b16 v[88:89], v157 offset:34848
	ds_read_b64_tr_b16 v[90:91], v157 offset:35936
	ds_read_b64_tr_b16 v[104:105], v157 offset:34880
	ds_read_b64_tr_b16 v[106:107], v157 offset:35968
	ds_read_b64_tr_b16 v[108:109], v157 offset:34912
	ds_read_b64_tr_b16 v[110:111], v157 offset:36000
	v_add_u32_e32 v182, v149, v158
	v_mov_b32_e32 v4, s72
	s_waitcnt lgkmcnt(6)
	v_mfma_f32_16x16x32_bf16 v[32:35], v[80:83], v[84:87], v[32:35]
	ds_read_b64_tr_b16 v[84:85], v157 offset:34944
	ds_read_b64_tr_b16 v[86:87], v157 offset:36032
	s_waitcnt lgkmcnt(6)
	v_mfma_f32_16x16x32_bf16 v[36:39], v[80:83], v[88:91], v[36:39]
	ds_read_b64_tr_b16 v[88:89], v157 offset:34976
	ds_read_b64_tr_b16 v[90:91], v157 offset:36064
	s_waitcnt lgkmcnt(6)
	v_mfma_f32_16x16x32_bf16 v[40:43], v[80:83], v[104:107], v[40:43]
	ds_read_b64_tr_b16 v[104:105], v157 offset:35008
	ds_read_b64_tr_b16 v[106:107], v157 offset:36096
	s_waitcnt lgkmcnt(6)
	v_mfma_f32_16x16x32_bf16 v[44:47], v[80:83], v[108:111], v[44:47]
	ds_read_b64_tr_b16 v[108:109], v157 offset:35040
	ds_read_b64_tr_b16 v[110:111], v157 offset:36128
	s_waitcnt lgkmcnt(6)
	v_mfma_f32_16x16x32_bf16 v[48:51], v[80:83], v[84:87], v[48:51]
	ds_read_b64_tr_b16 v[84:85], v182 offset:52224
	ds_read_b64_tr_b16 v[86:87], v182 offset:52352
	s_waitcnt lgkmcnt(6)
	v_mfma_f32_16x16x32_bf16 v[52:55], v[80:83], v[88:91], v[52:55]
	ds_read_b64_tr_b16 v[92:93], v196 offset:17408
	ds_read_b64_tr_b16 v[94:95], v196 offset:18496
	s_waitcnt lgkmcnt(6)
	v_mfma_f32_16x16x32_bf16 v[56:59], v[80:83], v[104:107], v[56:59]
	ds_read_b64_tr_b16 v[88:89], v160 offset:34816
	ds_read_b64_tr_b16 v[90:91], v160 offset:35904
	s_waitcnt lgkmcnt(6)
	v_mfma_f32_16x16x32_bf16 v[60:63], v[80:83], v[108:111], v[60:63]
	ds_read_b64_tr_b16 v[104:105], v160 offset:34848
	ds_read_b64_tr_b16 v[106:107], v160 offset:35936
	s_waitcnt lgkmcnt(6)
	v_mfma_f32_16x16x32_bf16 v[64:67], v[80:83], v[84:87], v[64:67]
	ds_read_b64_tr_b16 v[108:109], v160 offset:34880
	ds_read_b64_tr_b16 v[110:111], v160 offset:35968
	s_waitcnt lgkmcnt(4)
	v_mfma_f32_16x16x32_bf16 v[32:35], v[92:95], v[88:91], v[32:35]
	ds_read_b64_tr_b16 v[84:85], v160 offset:34912
	ds_read_b64_tr_b16 v[86:87], v160 offset:36000
	s_waitcnt lgkmcnt(4)
	v_mfma_f32_16x16x32_bf16 v[36:39], v[92:95], v[104:107], v[36:39]
	ds_read_b64_tr_b16 v[88:89], v160 offset:34944
	ds_read_b64_tr_b16 v[90:91], v160 offset:36032
	s_waitcnt lgkmcnt(4)
	v_mfma_f32_16x16x32_bf16 v[40:43], v[92:95], v[108:111], v[40:43]
	ds_read_b64_tr_b16 v[104:105], v160 offset:34976
	ds_read_b64_tr_b16 v[106:107], v160 offset:36064
	s_waitcnt lgkmcnt(4)
	v_mfma_f32_16x16x32_bf16 v[44:47], v[92:95], v[84:87], v[44:47]
	ds_read_b64_tr_b16 v[108:109], v160 offset:35008
	ds_read_b64_tr_b16 v[110:111], v160 offset:36096
	s_waitcnt lgkmcnt(4)
	v_mfma_f32_16x16x32_bf16 v[48:51], v[92:95], v[88:91], v[48:51]
	ds_read_b64_tr_b16 v[84:85], v160 offset:35040
	ds_read_b64_tr_b16 v[86:87], v160 offset:36128
	s_waitcnt lgkmcnt(4)
	v_mfma_f32_16x16x32_bf16 v[52:55], v[92:95], v[104:107], v[52:55]
	ds_read_b64_tr_b16 v[88:89], v177 offset:52224
	ds_read_b64_tr_b16 v[90:91], v177 offset:52352
	s_waitcnt lgkmcnt(4)
	v_mfma_f32_16x16x32_bf16 v[56:59], v[92:95], v[108:111], v[56:59]
	s_waitcnt lgkmcnt(2)
	v_mfma_f32_16x16x32_bf16 v[60:63], v[92:95], v[84:87], v[60:63]
	ds_read_b32 v4, v4
	s_waitcnt lgkmcnt(0)
	s_barrier
	v_mfma_f32_16x16x32_bf16 v[64:67], v[92:95], v[88:91], v[64:67]
	ds_read_b128 v[80:83], v6
	ds_read_b128 v[84:87], v197
	s_waitcnt lgkmcnt(0)
	v_max_f32_e64 v6, |v84|, |v84|
	v_max_f32_e32 v6, 1.0, v6
	v_rcp_f32_e32 v6, v6
	s_nop 0
	v_mul_f32_e32 v6, v80, v6
	v_mul_f32_e32 v92, v72, v6
	v_mul_f32_e32 v94, v68, v6
	v_cndmask_b32_e64 v68, 0, v92, s[20:21]
	v_cndmask_b32_e64 v7, 0, v94, s[20:21]
	v_mul_f32_e32 v68, v68, v68
	v_fmac_f32_e32 v68, v7, v7
	v_mul_f32_e32 v7, v96, v6
	v_cndmask_b32_e64 v72, 0, v7, s[20:21]
	v_mul_f32_e32 v84, v100, v6
	v_fmac_f32_e32 v68, v72, v72
	v_cndmask_b32_e64 v72, 0, v84, s[24:25]
	v_fmac_f32_e32 v68, v72, v72
	v_mul_f32_e32 v88, v76, v6
	v_fma_f32 v6, v88, v88, v68
	v_cndmask_b32_e64 v6, v68, v6, s[24:25]
	ds_bpermute_b32 v68, v179, v6
	s_waitcnt lgkmcnt(0)
	v_add_f32_e32 v6, v6, v68
	ds_bpermute_b32 v68, v180, v6
	s_waitcnt lgkmcnt(0)
	v_add_f32_e32 v6, v6, v68
	ds_bpermute_b32 v68, v181, v6
	s_waitcnt lgkmcnt(0)
	v_add_f32_e32 v68, v6, v68
	ds_bpermute_b32 v72, v131, v68
	v_add_u32_e32 v6, s42, v147
	s_and_saveexec_b64 s[30:31], s[4:5]
	s_cbranch_execz .LBB0_496
	s_waitcnt lgkmcnt(0)
	v_add_f32_e32 v68, v68, v72
	ds_write_b32 v6, v68

; #define WG_BAR() do { asm volatile("s_waitcnt lgkmcnt(0)" ::: "memory"); __builtin_amdgcn_s_barrier(); asm volatile("" ::: "memory"); } while (0)
; template <bool OUT, bool PASS2>
; __device__ __forceinline__ void ml_block(const Args& a, unsigned char* lds_g, int rowbase, int h, int dir, f32x4 (&st)[9], int tid) {
;     ...
;             for (int ks = 0; ks < 2; ++ks) { const bf16x8_t kf = frag_tr(Ki, ML_STRIDE, 32 * ks, 16 * w, lane);
; #pragma unroll
;                 for (int vt = 0; vt < 8; ++vt) st[vt] = __builtin_amdgcn_mfma_f32_16x16x32_bf16(kf, frag_tr(Vi, ML_STRIDE, 32 * ks, 16 * vt, lane), st[vt], 0, 0, 0);
;                 st[8] = __builtin_amdgcn_mfma_f32_16x16x32_bf16(kf, frag_tr(AUGi, 16, 32 * ks, 0, lane), st[8], 0, 0, 0); }
;             const float ee = ebend[c];
; #pragma unroll
;             for (int vt = 0; vt < 9; ++vt) st[vt] = st[vt] * ee;
;         }
;         WG_BAR();
;         if (OUT) {
;             float sq[4] = {0.f, 0.f, 0.f, 0.f};
; #pragma unroll
;             for (int r = 0; r < 4; ++r) { const int t = 16 * ti + 4 * fq + r; const float sc = eb[64 * c + t] * __builtin_amdgcn_rcpf(fmaxf(fabsf(den[t]), 1.f));
; #pragma unroll
;                 for (int x = 0; x < 4; ++x) { const int vt = vh * 5 + x; const float hv = (vt < 8) ? X[x][r] * sc : 0.f; hval[x][r] = hv; sq[r] += hv * hv; }
;                 if (vh == 0) { const float hv = X[4][r] * sc; X[4][r] = hv; sq[r] += hv * hv; } }
; #pragma unroll
;             for (int r = 0; r < 4; ++r) { float v = sq[r]; v += __shfl_xor(v, 1); v += __shfl_xor(v, 2); v += __shfl_xor(v, 4); v += __shfl_xor(v, 8); if (fr == 0) ssq[vh * 64 + 16 * ti + 4 * fq + r] = v; }
.LBB0_604:
	s_or_b64 exec, exec, s[28:29]
	ds_read_b64_tr_b16 v[76:77], v191 offset:17408
	ds_read_b64_tr_b16 v[78:79], v191 offset:18496
	ds_read_b64_tr_b16 v[80:81], v157 offset:34816
	ds_read_b64_tr_b16 v[82:83], v157 offset:35904
	ds_read_b64_tr_b16 v[84:85], v157 offset:34848
	ds_read_b64_tr_b16 v[86:87], v157 offset:35936
	ds_read_b64_tr_b16 v[100:101], v157 offset:34880
	ds_read_b64_tr_b16 v[102:103], v157 offset:35968
	ds_read_b64_tr_b16 v[104:105], v157 offset:34912
	ds_read_b64_tr_b16 v[106:107], v157 offset:36000
	s_add_i32 s28, s1, 0
	v_mov_b32_e32 v4, s28
	s_waitcnt lgkmcnt(6)
	v_mfma_f32_16x16x32_bf16 v[36:39], v[76:79], v[80:83], v[36:39]
	ds_read_b64_tr_b16 v[80:81], v157 offset:34944
	ds_read_b64_tr_b16 v[82:83], v157 offset:36032
	s_waitcnt lgkmcnt(6)
	v_mfma_f32_16x16x32_bf16 v[40:43], v[76:79], v[84:87], v[40:43]
	ds_read_b64_tr_b16 v[84:85], v157 offset:34976
	ds_read_b64_tr_b16 v[86:87], v157 offset:36064
	s_waitcnt lgkmcnt(6)
	v_mfma_f32_16x16x32_bf16 v[44:47], v[76:79], v[100:103], v[44:47]
	ds_read_b64_tr_b16 v[100:101], v157 offset:35008
	ds_read_b64_tr_b16 v[102:103], v157 offset:36096
	s_waitcnt lgkmcnt(6)
	v_mfma_f32_16x16x32_bf16 v[48:51], v[76:79], v[104:107], v[48:51]
	ds_read_b64_tr_b16 v[104:105], v157 offset:35040
	ds_read_b64_tr_b16 v[106:107], v157 offset:36128
	s_waitcnt lgkmcnt(6)
	v_mfma_f32_16x16x32_bf16 v[52:55], v[76:79], v[80:83], v[52:55]
	ds_read_b64_tr_b16 v[80:81], v182 offset:52224
	ds_read_b64_tr_b16 v[82:83], v182 offset:52352
	s_waitcnt lgkmcnt(6)
	v_mfma_f32_16x16x32_bf16 v[56:59], v[76:79], v[84:87], v[56:59]
	ds_read_b64_tr_b16 v[88:89], v192 offset:17408
	ds_read_b64_tr_b16 v[90:91], v192 offset:18496
	s_waitcnt lgkmcnt(6)
	v_mfma_f32_16x16x32_bf16 v[60:63], v[76:79], v[100:103], v[60:63]
	ds_read_b64_tr_b16 v[84:85], v160 offset:34816
	ds_read_b64_tr_b16 v[86:87], v160 offset:35904
	s_waitcnt lgkmcnt(6)
	v_mfma_f32_16x16x32_bf16 v[64:67], v[76:79], v[104:107], v[64:67]
	ds_read_b64_tr_b16 v[100:101], v160 offset:34848
	ds_read_b64_tr_b16 v[102:103], v160 offset:35936
	s_waitcnt lgkmcnt(6)
	v_mfma_f32_16x16x32_bf16 v[68:71], v[76:79], v[80:83], v[68:71]
	ds_read_b64_tr_b16 v[104:105], v160 offset:34880
	ds_read_b64_tr_b16 v[106:107], v160 offset:35968
	s_waitcnt lgkmcnt(4)
	v_mfma_f32_16x16x32_bf16 v[36:39], v[88:91], v[84:87], v[36:39]
	ds_read_b64_tr_b16 v[80:81], v160 offset:34912
	ds_read_b64_tr_b16 v[82:83], v160 offset:36000
	s_waitcnt lgkmcnt(4)
	v_mfma_f32_16x16x32_bf16 v[40:43], v[88:91], v[100:103], v[40:43]
	ds_read_b64_tr_b16 v[84:85], v160 offset:34944
	ds_read_b64_tr_b16 v[86:87], v160 offset:36032
	s_waitcnt lgkmcnt(4)
	v_mfma_f32_16x16x32_bf16 v[44:47], v[88:91], v[104:107], v[44:47]
	ds_read_b64_tr_b16 v[100:101], v160 offset:34976
	ds_read_b64_tr_b16 v[102:103], v160 offset:36064
	s_waitcnt lgkmcnt(4)
	v_mfma_f32_16x16x32_bf16 v[48:51], v[88:91], v[80:83], v[48:51]
	ds_read_b64_tr_b16 v[104:105], v160 offset:35008
	ds_read_b64_tr_b16 v[106:107], v160 offset:36096
	s_waitcnt lgkmcnt(4)
	v_mfma_f32_16x16x32_bf16 v[52:55], v[88:91], v[84:87], v[52:55]
	ds_read_b64_tr_b16 v[80:81], v160 offset:35040
	ds_read_b64_tr_b16 v[82:83], v160 offset:36128
	s_waitcnt lgkmcnt(4)
	v_mfma_f32_16x16x32_bf16 v[56:59], v[88:91], v[100:103], v[56:59]
	ds_read_b64_tr_b16 v[84:85], v177 offset:52224
	ds_read_b64_tr_b16 v[86:87], v177 offset:52352
	s_waitcnt lgkmcnt(4)
	v_mfma_f32_16x16x32_bf16 v[60:63], v[88:91], v[104:107], v[60:63]
	s_waitcnt lgkmcnt(2)
	v_mfma_f32_16x16x32_bf16 v[64:67], v[88:91], v[80:83], v[64:67]
	ds_read_b32 v4, v4
	s_waitcnt lgkmcnt(0)
	s_barrier
	v_mfma_f32_16x16x32_bf16 v[68:71], v[88:91], v[84:87], v[68:71]
	ds_read_b128 v[76:79], v6
	ds_read_b128 v[80:83], v193
	s_waitcnt lgkmcnt(0)
	v_max_f32_e64 v6, |v80|, |v80|
	v_max_f32_e32 v6, 1.0, v6
	v_rcp_f32_e32 v6, v6
	s_nop 0
	v_mul_f32_e32 v6, v76, v6
	v_mul_f32_e32 v90, v72, v6
	v_mul_f32_e32 v91, v0, v6
	v_cndmask_b32_e64 v7, 0, v90, s[20:21]
	v_cndmask_b32_e64 v0, 0, v91, s[20:21]
	v_mul_f32_e32 v7, v7, v7
	v_mul_f32_e32 v89, v96, v6
	v_fmac_f32_e32 v7, v0, v0
	v_cndmask_b32_e64 v0, 0, v89, s[20:21]
	v_mul_f32_e32 v84, v108, v6
	v_fmac_f32_e32 v7, v0, v0
	v_cndmask_b32_e64 v0, 0, v84, s[24:25]
	v_fmac_f32_e32 v7, v0, v0
	v_mul_f32_e32 v88, v92, v6
	v_fma_f32 v0, v88, v88, v7
	v_cndmask_b32_e64 v0, v7, v0, s[24:25]
	ds_bpermute_b32 v6, v179, v0
	s_waitcnt lgkmcnt(0)
	v_add_f32_e32 v0, v0, v6
	ds_bpermute_b32 v6, v180, v0
	s_waitcnt lgkmcnt(0)
	v_add_f32_e32 v0, v0, v6
	ds_bpermute_b32 v6, v181, v0
	s_waitcnt lgkmcnt(0)
	v_add_f32_e32 v6, v0, v6
	ds_bpermute_b32 v7, v131, v6
	v_add_u32_e32 v0, s40, v147
	s_and_saveexec_b64 s[28:29], s[4:5]
	s_cbranch_execz .LBB0_606
	s_waitcnt lgkmcnt(0)
	v_add_f32_e32 v6, v6, v7
	ds_write_b32 v0, v6
